# v27 + RG-LRU next-chunk row prefetch: 8 exec-masked conditional loads (~180 instr) replaced by 8 range-checked buffer loads through a per-sequence SRD (~45 instr), both passes
# speedup vs baseline: 1.0167x; 1.0167x over previous
; #define LAS __attribute__((address_space(3)))
; #define LDS_BARRIER() do { asm volatile("s_waitcnt lgkmcnt(0)" ::: "memory"); __builtin_amdgcn_s_barrier(); asm volatile("" ::: "memory"); } while (0)
; __device__ __forceinline__ unsigned pk2(float lo, float hi) { return pg8::cvt_pk_bf16(lo, hi); }
; template <bool FINAL> __device__ __forceinline__ void rglru_pass(Frame& F) {
;     ...
;     for (int c = cg; c < nch; c += ncg) {
;         const int row0 = c < 256 ? c * 64 : ML + (c - 256) * 64;
;         LDS_BARRIER();
; #pragma unroll
;         for (int it = 0; it < 2; ++it) { const int id = F.tid + 512 * it, t = id >> 4, c8 = (id & 15) * 8;
;             float a[8];
;             { const f32x4 b0 = *(const LAS f32x4*)(CWL + 512 + c8), b1 = *(const LAS f32x4*)(CWL + 512 + c8 + 4);
;               a[0] = b0.x; a[1] = b0.y; a[2] = b0.z; a[3] = b0.w; a[4] = b1.x; a[5] = b1.y; a[6] = b1.z; a[7] = b1.w; }
; #pragma unroll
;             for (int tap = 0; tap < 4; ++tap) { const v4u x = xq[it][tap];
;                 const f32x4 w0 = *(const LAS f32x4*)(CWL + tap * 128 + c8), w1 = *(const LAS f32x4*)(CWL + tap * 128 + c8 + 4);
;                 a[0] += w0.x * bflo(x[0]); a[1] += w0.y * bfhi(x[0]); a[2] += w0.z * bflo(x[1]); a[3] += w0.w * bfhi(x[1]);
;                 a[4] += w1.x * bflo(x[2]); a[5] += w1.y * bfhi(x[2]); a[6] += w1.z * bflo(x[3]); a[7] += w1.w * bfhi(x[3]); }
;             *(LAS f32x4*)(XCF + t * 128 + c8) = (f32x4){a[0], a[1], a[2], a[3]}; *(LAS f32x4*)(XCF + t * 128 + c8 + 4) = (f32x4){a[4], a[5], a[6], a[7]};
;             v4u w; w.x = pk2(a[0], a[1]); w.y = pk2(a[2], a[3]); w.z = pk2(a[4], a[5]); w.w = pk2(a[6], a[7]);
;             *(LAS v4u*)(XCB + t * 272 + c8 * 2) = w; }
;         LDS_BARRIER();
;         if (c + ncg < nch) RG_LOAD_ROWS(c + ncg);
.LBB0_1392:
	s_waitcnt lgkmcnt(0)
	s_barrier
	s_waitcnt lgkmcnt(0)
	ds_read_b128 v[34:37], v167
	ds_read_b128 v[38:41], v167 offset:16
	ds_read_b128 v[42:45], v176
	ds_read_b128 v[46:49], v176 offset:16
	ds_read_b128 v[50:53], v176 offset:512
	ds_read_b128 v[54:57], v176 offset:528
	ds_read_b128 v[58:61], v176 offset:1024
	ds_read_b128 v[62:65], v176 offset:1040
	ds_read_b128 v[170:173], v176 offset:1536
	ds_read_b128 v[188:191], v176 offset:1552
	s_waitcnt vmcnt(0)
	v_lshlrev_b32_e32 v174, 16, v134
	v_and_b32_e32 v175, 0xffff0000, v134
	s_waitcnt lgkmcnt(7)
	v_pk_fma_f32 v[34:35], v[42:43], v[174:175], v[34:35]
	v_lshlrev_b32_e32 v42, 16, v130
	v_and_b32_e32 v43, 0xffff0000, v130
	s_waitcnt lgkmcnt(5)
	v_pk_fma_f32 v[34:35], v[50:51], v[42:43], v[34:35]
	v_lshlrev_b32_e32 v42, 16, v138
	v_and_b32_e32 v43, 0xffff0000, v138
	s_waitcnt lgkmcnt(3)
	v_pk_fma_f32 v[34:35], v[58:59], v[42:43], v[34:35]
	v_lshlrev_b32_e32 v42, 16, v142
	v_and_b32_e32 v43, 0xffff0000, v142
	s_waitcnt lgkmcnt(1)
	v_pk_fma_f32 v[34:35], v[170:171], v[42:43], v[34:35]
	v_lshlrev_b32_e32 v42, 16, v135
	v_and_b32_e32 v43, 0xffff0000, v135
	v_pk_fma_f32 v[36:37], v[44:45], v[42:43], v[36:37]
	v_lshlrev_b32_e32 v42, 16, v131
	v_and_b32_e32 v43, 0xffff0000, v131
	v_pk_fma_f32 v[36:37], v[52:53], v[42:43], v[36:37]
	v_lshlrev_b32_e32 v42, 16, v139
	v_and_b32_e32 v43, 0xffff0000, v139
	v_pk_fma_f32 v[36:37], v[60:61], v[42:43], v[36:37]
	v_lshlrev_b32_e32 v42, 16, v143
	v_and_b32_e32 v43, 0xffff0000, v143
	v_pk_fma_f32 v[36:37], v[172:173], v[42:43], v[36:37]
	v_lshlrev_b32_e32 v42, 16, v136
	v_and_b32_e32 v43, 0xffff0000, v136
	v_pk_fma_f32 v[38:39], v[46:47], v[42:43], v[38:39]
	v_lshlrev_b32_e32 v42, 16, v132
	v_and_b32_e32 v43, 0xffff0000, v132
	v_pk_fma_f32 v[38:39], v[54:55], v[42:43], v[38:39]
	v_lshlrev_b32_e32 v42, 16, v140
	v_and_b32_e32 v43, 0xffff0000, v140
	v_pk_fma_f32 v[38:39], v[62:63], v[42:43], v[38:39]
	v_lshlrev_b32_e32 v42, 16, v144
	v_and_b32_e32 v43, 0xffff0000, v144
	s_waitcnt lgkmcnt(0)
	v_pk_fma_f32 v[38:39], v[188:189], v[42:43], v[38:39]
	v_lshlrev_b32_e32 v42, 16, v137
	v_and_b32_e32 v43, 0xffff0000, v137
	v_pk_fma_f32 v[40:41], v[48:49], v[42:43], v[40:41]
	v_lshlrev_b32_e32 v42, 16, v133
	v_and_b32_e32 v43, 0xffff0000, v133
	v_pk_fma_f32 v[40:41], v[56:57], v[42:43], v[40:41]
	v_lshlrev_b32_e32 v42, 16, v141
	v_and_b32_e32 v43, 0xffff0000, v141
	v_pk_fma_f32 v[40:41], v[64:65], v[42:43], v[40:41]
	v_lshlrev_b32_e32 v42, 16, v145
	v_and_b32_e32 v43, 0xffff0000, v145
	v_pk_fma_f32 v[40:41], v[190:191], v[42:43], v[40:41]
	ds_write_b128 v177, v[34:37] offset:17408
	ds_write_b128 v177, v[38:41] offset:17424
	v_cvt_pk_bf16_f32 v34, v34, v35
	v_cvt_pk_bf16_f32 v35, v36, v37
	v_cvt_pk_bf16_f32 v36, v38, v39
	v_cvt_pk_bf16_f32 v37, v40, v41
	ds_write_b128 v182, v[34:37]
	ds_read_b128 v[34:37], v167
	ds_read_b128 v[38:41], v167 offset:16
	ds_read_b128 v[42:45], v176
	ds_read_b128 v[46:49], v176 offset:16
	ds_read_b128 v[50:53], v176 offset:512
	ds_read_b128 v[54:57], v176 offset:528
	ds_read_b128 v[58:61], v176 offset:1024
	ds_read_b128 v[62:65], v176 offset:1040
	ds_read_b128 v[170:173], v176 offset:1536
	ds_read_b128 v[188:191], v176 offset:1552
	v_lshlrev_b32_e32 v174, 16, v146
	v_and_b32_e32 v175, 0xffff0000, v146
	s_waitcnt lgkmcnt(7)
	v_pk_fma_f32 v[34:35], v[42:43], v[174:175], v[34:35]
	v_lshlrev_b32_e32 v42, 16, v150
	v_and_b32_e32 v43, 0xffff0000, v150
	s_waitcnt lgkmcnt(5)
	v_pk_fma_f32 v[34:35], v[50:51], v[42:43], v[34:35]
	v_lshlrev_b32_e32 v42, 16, v156
	v_and_b32_e32 v43, 0xffff0000, v156
	s_waitcnt lgkmcnt(3)
	v_pk_fma_f32 v[34:35], v[58:59], v[42:43], v[34:35]
	v_lshlrev_b32_e32 v42, 16, v160
	v_and_b32_e32 v43, 0xffff0000, v160
	s_waitcnt lgkmcnt(1)
	v_pk_fma_f32 v[34:35], v[170:171], v[42:43], v[34:35]
	v_lshlrev_b32_e32 v42, 16, v147
	v_and_b32_e32 v43, 0xffff0000, v147
	v_pk_fma_f32 v[36:37], v[44:45], v[42:43], v[36:37]
	v_lshlrev_b32_e32 v42, 16, v151
	v_and_b32_e32 v43, 0xffff0000, v151
	v_pk_fma_f32 v[36:37], v[52:53], v[42:43], v[36:37]
	v_lshlrev_b32_e32 v42, 16, v157
	v_and_b32_e32 v43, 0xffff0000, v157
	v_pk_fma_f32 v[36:37], v[60:61], v[42:43], v[36:37]
	v_lshlrev_b32_e32 v42, 16, v161
	v_and_b32_e32 v43, 0xffff0000, v161
	v_pk_fma_f32 v[36:37], v[172:173], v[42:43], v[36:37]
	v_lshlrev_b32_e32 v42, 16, v148
	v_and_b32_e32 v43, 0xffff0000, v148
	v_pk_fma_f32 v[38:39], v[46:47], v[42:43], v[38:39]
	v_lshlrev_b32_e32 v42, 16, v152
	v_and_b32_e32 v43, 0xffff0000, v152
	v_pk_fma_f32 v[38:39], v[54:55], v[42:43], v[38:39]
	v_lshlrev_b32_e32 v42, 16, v158
	v_and_b32_e32 v43, 0xffff0000, v158
	v_pk_fma_f32 v[38:39], v[62:63], v[42:43], v[38:39]
	v_lshlrev_b32_e32 v42, 16, v162
	v_and_b32_e32 v43, 0xffff0000, v162
	s_waitcnt lgkmcnt(0)
	v_pk_fma_f32 v[38:39], v[188:189], v[42:43], v[38:39]
	v_lshlrev_b32_e32 v42, 16, v149
	v_and_b32_e32 v43, 0xffff0000, v149
	v_pk_fma_f32 v[40:41], v[48:49], v[42:43], v[40:41]
	v_lshlrev_b32_e32 v42, 16, v153
	v_and_b32_e32 v43, 0xffff0000, v153
	v_pk_fma_f32 v[40:41], v[56:57], v[42:43], v[40:41]
	v_lshlrev_b32_e32 v42, 16, v159
	v_and_b32_e32 v43, 0xffff0000, v159
	v_pk_fma_f32 v[40:41], v[64:65], v[42:43], v[40:41]
	v_lshlrev_b32_e32 v42, 16, v163
	v_and_b32_e32 v43, 0xffff0000, v163
	v_pk_fma_f32 v[40:41], v[190:191], v[42:43], v[40:41]
	ds_write_b128 v181, v[34:37] offset:17408
	ds_write_b128 v181, v[38:41] offset:17424
	v_cvt_pk_bf16_f32 v34, v34, v35
	v_cvt_pk_bf16_f32 v35, v36, v37
	v_cvt_pk_bf16_f32 v36, v38, v39
	v_cvt_pk_bf16_f32 v37, v40, v41
	ds_write_b128 v183, v[34:37]
	s_add_i32 s12, s12, s14
	s_waitcnt lgkmcnt(0)
	s_barrier
	s_cmpk_gt_i32 s12, 0x107
	s_cselect_b64 s[22:23], -1, 0
	s_and_b64 vcc, exec, s[22:23]
	s_cbranch_vccnz .LBB0_1410
	s_cmpk_lt_i32 s12, 0x100
	s_cselect_b32 s7, s24, 0xffffff00
	s_cselect_b32 s6, s21, 0x100
	s_and_b32 s25, s7, s13
	s_mov_b32 s76, s25
	s_mov_b32 s77, 0
	s_lshl_b64 s[76:77], s[76:77], 13
	s_add_u32 s76, s76, 0x1000
	s_addc_u32 s77, s77, 0
	s_add_u32 s68, s8, s76
	s_addc_u32 s69, s9, s77
	s_and_b32 s69, s69, 0xffff
	s_lshl_b32 s70, s6, 13
	s_sub_u32 s70, s70, 0x1000
	s_mov_b32 s71, 0x20000
	s_sub_i32 s78, s13, s25
	s_add_i32 s78, s78, -2
	v_lshlrev_b32_e32 v38, 1, v166
	v_add_u32_e32 v34, s78, v1
	v_lshl_add_u32 v34, v34, 13, v38
	buffer_load_dwordx4 v[134:137], v34, s[68:71], 0 offen
	v_add_u32_e32 v35, 0x2000, v34
	buffer_load_dwordx4 v[130:133], v35, s[68:71], 0 offen
	v_add_u32_e32 v36, 0x4000, v34
	buffer_load_dwordx4 v[138:141], v36, s[68:71], 0 offen
	v_add_u32_e32 v37, 0x6000, v34
	buffer_load_dwordx4 v[142:145], v37, s[68:71], 0 offen
	v_add_u32_e32 v34, s78, v179
	v_lshl_add_u32 v34, v34, 13, v38
	buffer_load_dwordx4 v[146:149], v34, s[68:71], 0 offen
	v_add_u32_e32 v35, 0x2000, v34
	buffer_load_dwordx4 v[150:153], v35, s[68:71], 0 offen
	v_add_u32_e32 v36, 0x4000, v34
	buffer_load_dwordx4 v[156:159], v36, s[68:71], 0 offen
	v_add_u32_e32 v37, 0x6000, v34
	buffer_load_dwordx4 v[160:163], v37, s[68:71], 0 offen
	v_mov_b32_e32 v155, v154

; #define LAS __attribute__((address_space(3)))
; #define LDS_BARRIER() do { asm volatile("s_waitcnt lgkmcnt(0)" ::: "memory"); __builtin_amdgcn_s_barrier(); asm volatile("" ::: "memory"); } while (0)
; __device__ __forceinline__ unsigned pk2(float lo, float hi) { return pg8::cvt_pk_bf16(lo, hi); }
; template <bool FINAL> __device__ __forceinline__ void rglru_pass(Frame& F) {
;     ...
;     for (int c = cg; c < nch; c += ncg) {
;         const int row0 = c < 256 ? c * 64 : ML + (c - 256) * 64;
;         LDS_BARRIER();
; #pragma unroll
;         for (int it = 0; it < 2; ++it) { const int id = F.tid + 512 * it, t = id >> 4, c8 = (id & 15) * 8;
;             float a[8];
;             { const f32x4 b0 = *(const LAS f32x4*)(CWL + 512 + c8), b1 = *(const LAS f32x4*)(CWL + 512 + c8 + 4);
;               a[0] = b0.x; a[1] = b0.y; a[2] = b0.z; a[3] = b0.w; a[4] = b1.x; a[5] = b1.y; a[6] = b1.z; a[7] = b1.w; }
; #pragma unroll
;             for (int tap = 0; tap < 4; ++tap) { const v4u x = xq[it][tap];
;                 const f32x4 w0 = *(const LAS f32x4*)(CWL + tap * 128 + c8), w1 = *(const LAS f32x4*)(CWL + tap * 128 + c8 + 4);
;                 a[0] += w0.x * bflo(x[0]); a[1] += w0.y * bfhi(x[0]); a[2] += w0.z * bflo(x[1]); a[3] += w0.w * bfhi(x[1]);
;                 a[4] += w1.x * bflo(x[2]); a[5] += w1.y * bfhi(x[2]); a[6] += w1.z * bflo(x[3]); a[7] += w1.w * bfhi(x[3]); }
;             *(LAS f32x4*)(XCF + t * 128 + c8) = (f32x4){a[0], a[1], a[2], a[3]}; *(LAS f32x4*)(XCF + t * 128 + c8 + 4) = (f32x4){a[4], a[5], a[6], a[7]};
;             v4u w; w.x = pk2(a[0], a[1]); w.y = pk2(a[2], a[3]); w.z = pk2(a[4], a[5]); w.w = pk2(a[6], a[7]);
;             *(LAS v4u*)(XCB + t * 272 + c8 * 2) = w; }
;         LDS_BARRIER();
;         if (c + ncg < nch) RG_LOAD_ROWS(c + ncg);
.LBB0_1585:
	s_waitcnt lgkmcnt(0)
	s_barrier
	ds_read_b128 v[34:37], v179
	ds_read_b128 v[38:41], v179 offset:16
	ds_read_b128 v[42:45], v181
	ds_read_b128 v[46:49], v181 offset:16
	ds_read_b128 v[50:53], v181 offset:512
	ds_read_b128 v[54:57], v181 offset:528
	ds_read_b128 v[58:61], v181 offset:1024
	ds_read_b128 v[62:65], v181 offset:1040
	ds_read_b128 v[164:167], v181 offset:1536
	ds_read_b128 v[168:171], v181 offset:1552
	s_waitcnt vmcnt(0)
	v_lshlrev_b32_e32 v190, 16, v134
	v_and_b32_e32 v191, 0xffff0000, v134
	s_waitcnt lgkmcnt(7)
	v_pk_fma_f32 v[34:35], v[42:43], v[190:191], v[34:35]
	v_lshlrev_b32_e32 v42, 16, v130
	v_and_b32_e32 v43, 0xffff0000, v130
	s_waitcnt lgkmcnt(5)
	v_pk_fma_f32 v[34:35], v[50:51], v[42:43], v[34:35]
	v_lshlrev_b32_e32 v42, 16, v138
	v_and_b32_e32 v43, 0xffff0000, v138
	s_waitcnt lgkmcnt(3)
	v_pk_fma_f32 v[34:35], v[58:59], v[42:43], v[34:35]
	v_lshlrev_b32_e32 v42, 16, v142
	v_and_b32_e32 v43, 0xffff0000, v142
	s_waitcnt lgkmcnt(1)
	v_pk_fma_f32 v[34:35], v[164:165], v[42:43], v[34:35]
	v_lshlrev_b32_e32 v42, 16, v135
	v_and_b32_e32 v43, 0xffff0000, v135
	v_pk_fma_f32 v[36:37], v[44:45], v[42:43], v[36:37]
	v_lshlrev_b32_e32 v42, 16, v131
	v_and_b32_e32 v43, 0xffff0000, v131
	v_pk_fma_f32 v[36:37], v[52:53], v[42:43], v[36:37]
	v_lshlrev_b32_e32 v42, 16, v139
	v_and_b32_e32 v43, 0xffff0000, v139
	v_pk_fma_f32 v[36:37], v[60:61], v[42:43], v[36:37]
	v_lshlrev_b32_e32 v42, 16, v143
	v_and_b32_e32 v43, 0xffff0000, v143
	v_pk_fma_f32 v[36:37], v[166:167], v[42:43], v[36:37]
	v_lshlrev_b32_e32 v42, 16, v136
	v_and_b32_e32 v43, 0xffff0000, v136
	v_pk_fma_f32 v[38:39], v[46:47], v[42:43], v[38:39]
	v_lshlrev_b32_e32 v42, 16, v132
	v_and_b32_e32 v43, 0xffff0000, v132
	v_pk_fma_f32 v[38:39], v[54:55], v[42:43], v[38:39]
	v_lshlrev_b32_e32 v42, 16, v140
	v_and_b32_e32 v43, 0xffff0000, v140
	v_pk_fma_f32 v[38:39], v[62:63], v[42:43], v[38:39]
	v_lshlrev_b32_e32 v42, 16, v144
	v_and_b32_e32 v43, 0xffff0000, v144
	s_waitcnt lgkmcnt(0)
	v_pk_fma_f32 v[38:39], v[168:169], v[42:43], v[38:39]
	v_lshlrev_b32_e32 v42, 16, v137
	v_and_b32_e32 v43, 0xffff0000, v137
	v_pk_fma_f32 v[40:41], v[48:49], v[42:43], v[40:41]
	v_lshlrev_b32_e32 v42, 16, v133
	v_and_b32_e32 v43, 0xffff0000, v133
	v_pk_fma_f32 v[40:41], v[56:57], v[42:43], v[40:41]
	v_lshlrev_b32_e32 v42, 16, v141
	v_and_b32_e32 v43, 0xffff0000, v141
	v_pk_fma_f32 v[40:41], v[64:65], v[42:43], v[40:41]
	v_lshlrev_b32_e32 v42, 16, v145
	v_and_b32_e32 v43, 0xffff0000, v145
	v_pk_fma_f32 v[40:41], v[170:171], v[42:43], v[40:41]
	ds_write_b128 v201, v[34:37] offset:17408
	ds_write_b128 v201, v[38:41] offset:17424
	v_cvt_pk_bf16_f32 v34, v34, v35
	v_cvt_pk_bf16_f32 v35, v36, v37
	v_cvt_pk_bf16_f32 v36, v38, v39
	v_add_u32_e32 v38, v194, v186
	v_cvt_pk_bf16_f32 v37, v40, v41
	ds_write_b128 v38, v[34:37]
	ds_read_b128 v[34:37], v179
	ds_read_b128 v[38:41], v179 offset:16
	ds_read_b128 v[42:45], v181
	ds_read_b128 v[46:49], v181 offset:16
	ds_read_b128 v[50:53], v181 offset:512
	ds_read_b128 v[54:57], v181 offset:528
	ds_read_b128 v[58:61], v181 offset:1024
	ds_read_b128 v[62:65], v181 offset:1040
	ds_read_b128 v[164:167], v181 offset:1536
	ds_read_b128 v[168:171], v181 offset:1552
	v_lshlrev_b32_e32 v190, 16, v146
	v_and_b32_e32 v191, 0xffff0000, v146
	s_waitcnt lgkmcnt(7)
	v_pk_fma_f32 v[34:35], v[42:43], v[190:191], v[34:35]
	v_lshlrev_b32_e32 v42, 16, v150
	v_and_b32_e32 v43, 0xffff0000, v150
	s_waitcnt lgkmcnt(5)
	v_pk_fma_f32 v[34:35], v[50:51], v[42:43], v[34:35]
	v_lshlrev_b32_e32 v42, 16, v154
	v_and_b32_e32 v43, 0xffff0000, v154
	s_waitcnt lgkmcnt(3)
	v_pk_fma_f32 v[34:35], v[58:59], v[42:43], v[34:35]
	v_lshlrev_b32_e32 v42, 16, v160
	v_and_b32_e32 v43, 0xffff0000, v160
	s_waitcnt lgkmcnt(1)
	v_pk_fma_f32 v[34:35], v[164:165], v[42:43], v[34:35]
	v_lshlrev_b32_e32 v42, 16, v147
	v_and_b32_e32 v43, 0xffff0000, v147
	v_pk_fma_f32 v[36:37], v[44:45], v[42:43], v[36:37]
	v_lshlrev_b32_e32 v42, 16, v151
	v_and_b32_e32 v43, 0xffff0000, v151
	v_pk_fma_f32 v[36:37], v[52:53], v[42:43], v[36:37]
	v_lshlrev_b32_e32 v42, 16, v155
	v_and_b32_e32 v43, 0xffff0000, v155
	v_pk_fma_f32 v[36:37], v[60:61], v[42:43], v[36:37]
	v_lshlrev_b32_e32 v42, 16, v161
	v_and_b32_e32 v43, 0xffff0000, v161
	v_pk_fma_f32 v[36:37], v[166:167], v[42:43], v[36:37]
	v_lshlrev_b32_e32 v42, 16, v148
	v_and_b32_e32 v43, 0xffff0000, v148
	v_pk_fma_f32 v[38:39], v[46:47], v[42:43], v[38:39]
	v_lshlrev_b32_e32 v42, 16, v152
	v_and_b32_e32 v43, 0xffff0000, v152
	v_pk_fma_f32 v[38:39], v[54:55], v[42:43], v[38:39]
	v_lshlrev_b32_e32 v42, 16, v156
	v_and_b32_e32 v43, 0xffff0000, v156
	v_pk_fma_f32 v[38:39], v[62:63], v[42:43], v[38:39]
	v_lshlrev_b32_e32 v42, 16, v162
	v_and_b32_e32 v43, 0xffff0000, v162
	s_waitcnt lgkmcnt(0)
	v_pk_fma_f32 v[38:39], v[168:169], v[42:43], v[38:39]
	v_lshlrev_b32_e32 v42, 16, v149
	v_and_b32_e32 v43, 0xffff0000, v149
	v_pk_fma_f32 v[40:41], v[48:49], v[42:43], v[40:41]
	v_lshlrev_b32_e32 v42, 16, v153
	v_and_b32_e32 v43, 0xffff0000, v153
	v_pk_fma_f32 v[40:41], v[56:57], v[42:43], v[40:41]
	v_lshlrev_b32_e32 v42, 16, v157
	v_and_b32_e32 v43, 0xffff0000, v157
	v_pk_fma_f32 v[40:41], v[64:65], v[42:43], v[40:41]
	v_lshlrev_b32_e32 v42, 16, v163
	v_and_b32_e32 v43, 0xffff0000, v163
	v_pk_fma_f32 v[40:41], v[170:171], v[42:43], v[40:41]
	ds_write_b128 v202, v[34:37] offset:17408
	ds_write_b128 v202, v[38:41] offset:17424
	v_cvt_pk_bf16_f32 v34, v34, v35
	v_cvt_pk_bf16_f32 v35, v36, v37
	v_cvt_pk_bf16_f32 v36, v38, v39
	v_add_u32_e32 v38, v195, v186
	v_cvt_pk_bf16_f32 v37, v40, v41
	ds_write_b128 v38, v[34:37]
	s_waitcnt lgkmcnt(0)
	s_barrier
	s_add_i32 s4, s17, s22
	s_cmpk_gt_i32 s4, 0xff
	s_cbranch_scc1 .LBB0_1603
	s_add_i32 s4, s19, s15
	s_and_b32 s23, s4, 0xffffe000
	s_mov_b32 s76, s23
	s_mov_b32 s77, 0
	s_lshl_b64 s[76:77], s[76:77], 13
	s_add_u32 s76, s76, 0x1000
	s_addc_u32 s77, s77, 0
	s_add_u32 s68, s6, s76
	s_addc_u32 s69, s7, s77
	s_and_b32 s69, s69, 0xffff
	s_mov_b32 s70, 0x3fff000
	s_mov_b32 s71, 0x20000
	s_sub_i32 s78, s15, s23
	s_add_i32 s78, s78, -2
	v_add_u32_e32 v34, s78, v200
	v_lshl_add_u32 v34, v34, 13, v172
	buffer_load_dwordx4 v[134:137], v34, s[68:71], 0 offen
	v_add_u32_e32 v35, 0x2000, v34
	buffer_load_dwordx4 v[130:133], v35, s[68:71], 0 offen
	v_add_u32_e32 v36, 0x4000, v34
	buffer_load_dwordx4 v[138:141], v36, s[68:71], 0 offen
	v_add_u32_e32 v37, 0x6000, v34
	buffer_load_dwordx4 v[142:145], v37, s[68:71], 0 offen
	v_add_u32_e32 v34, s78, v199
	v_lshl_add_u32 v34, v34, 13, v172
	buffer_load_dwordx4 v[146:149], v34, s[68:71], 0 offen
	v_add_u32_e32 v35, 0x2000, v34
	buffer_load_dwordx4 v[150:153], v35, s[68:71], 0 offen
	v_add_u32_e32 v36, 0x4000, v34
	buffer_load_dwordx4 v[154:157], v36, s[68:71], 0 offen
	v_add_u32_e32 v37, 0x6000, v34
	buffer_load_dwordx4 v[160:163], v37, s[68:71], 0 offen
	v_mov_b32_e32 v159, v158
